# expert value-table 4-bit conversion moved from the attention phase work queue into the routing phase (loads fly under the routing work) on top of v3
# speedup vs baseline: 1.0095x; 1.0095x over previous
.Luv4_slot_written:
	s_or_b64 exec, exec, s[10:11]
	v_mov_b32_e32 v2, 0
	s_waitcnt lgkmcnt(0)
	s_barrier
	ds_read_b32 v2, v2
	s_mov_b64 s[10:11], -1
	s_waitcnt lgkmcnt(0)
	v_cmp_gt_u32_e32 vcc, 0x800, v2
	s_and_saveexec_b64 s[24:25], vcc
	s_cbranch_execz .LBB0_1388
	v_lshl_add_u32 v2, v2, 3, v72
	v_add_u32_e32 v3, 0xffffc000, v2
	v_cmp_lt_i32_e64 s[10:11], s37, v2
	v_mov_b32_e32 v4, s18
	s_nop 0
	v_cndmask_b32_e64 v70, v2, v3, s[10:11]
	v_mov_b32_e32 v2, s17
	v_mov_b32_e32 v3, s19
	v_cndmask_b32_e64 v3, v2, v3, s[10:11]
	v_mov_b32_e32 v2, s16
	v_ashrrev_i32_e32 v71, 31, v70
	v_cndmask_b32_e64 v2, v2, v4, s[10:11]
	v_lshlrev_b64 v[4:5], 14, v[70:71]
	v_lshl_add_u64 v[2:3], v[2:3], 0, v[4:5]
	v_lshl_add_u64 v[2:3], v[2:3], 0, v[66:67]
	s_and_saveexec_b64 s[98:99], s[6:7]
	s_cbranch_execz .Luv4_next_issued
	v_mov_b32_e32 v250, 1
	global_atomic_add v250, v67, v250, s[20:21] sc0

.LBB0_1806:
	s_or_b64 exec, exec, s[12:13]
	s_cmpk_gt_u32 s2, 0x7ff
	s_cbranch_scc1 .LBB0_1936
	s_add_u32 s42, s8, 0x40400000
	s_addc_u32 s43, s9, 0
	s_add_u32 s50, s10, 4.0
	s_addc_u32 s51, s11, 0
	s_ashr_i32 s8, s18, 6
	s_lshr_b32 s47, s2, 3
	s_lshl_b32 s9, s3, 9
	v_and_b32_e32 v35, 15, v5
	s_add_u32 s6, s6, s9
	s_addc_u32 s7, s7, 0
	v_lshlrev_b32_e32 v36, 5, v35
	v_mov_b32_e32 v37, 0
	v_lshl_add_u64 v[2:3], s[6:7], 0, v[36:37]
	s_mov_b64 s[6:7], 0x38400000
	v_ashrrev_i32_e32 v72, 4, v5
	v_lshl_add_u64 v[38:39], v[2:3], 0, s[6:7]
	s_movk_i32 s6, 0x210
	v_mul_lo_u32 v2, v72, s6
	s_add_i32 s6, 0, 0x11000
	v_and_b32_e32 v4, 48, v5
	v_add_u32_e32 v2, s6, v2
	v_add_u32_e32 v6, 0, v4
	v_add_u32_e32 v4, s6, v4
	s_lshl_b32 s6, s8, 10
	s_add_i32 s6, s6, 0
	v_lshrrev_b32_e32 v7, 2, v5
	s_add_i32 s6, s6, 0x1d600
	v_bfe_u32 v5, v5, 4, 2
	v_lshl_add_u32 v73, v5, 8, s6
	v_lshl_or_b32 v74, s8, 2, v5
	s_movk_i32 s6, 0x420
	v_lshl_or_b32 v3, s8, 4, v35
	v_and_b32_e32 v7, 12, v7
	v_mul_lo_u32 v5, v74, s6
	s_add_i32 s6, 0, 0x15200
	v_lshlrev_b32_e32 v8, 2, v35
	s_movk_i32 s7, 0x110
	v_add3_u32 v75, s6, v5, v8
	v_lshlrev_b32_e32 v5, 3, v35
	v_mul_lo_u32 v8, v3, s7
	v_lshl_add_u32 v3, v3, 2, s6
	v_mul_u32_u24_e32 v9, 0x210, v35
	v_mul_u32_u24_e32 v7, 0x420, v7
	s_lshl_b32 s52, s3, 4
	v_or_b32_e32 v41, 16, v35
	v_or_b32_e32 v43, 32, v35
	v_or_b32_e32 v45, 48, v35
	v_or_b32_e32 v47, 64, v35
	v_or_b32_e32 v49, 0x50, v35
	v_or_b32_e32 v51, 0x60, v35
	v_or_b32_e32 v53, 0x70, v35
	s_lshr_b32 s53, s46, 3
	v_add_u32_e32 v76, v2, v36
	v_add_u32_e32 v77, v6, v8
	v_add_u32_e32 v78, v4, v9
	v_add_u32_e32 v79, v3, v7
	v_add_u32_e32 v80, v73, v5
	s_mov_b32 s54, 0x800000
	s_mov_b32 s55, 0xff000000
	s_load_dwordx2 s[94:95], s[0:1], 0x80
	s_load_dwordx2 s[96:97], s[0:1], 0x90
	v_lshlrev_b32_e32 v226, 4, v1
	v_mov_b32_e32 v227, 0
	v_lshlrev_b32_e32 v228, 2, v1
	v_ashrrev_i32_e32 v232, 6, v0
	v_mov_b32_e32 v233, 0x260
	v_mov_b32_e32 v234, 0x41700000
	s_waitcnt lgkmcnt(0)
	s_add_u32 s98, s96, 0x16300000
	s_addc_u32 s99, s97, 0
	s_add_u32 s96, s96, 0x12300000
	s_addc_u32 s97, s97, 0
	s_branch .LBB0_1809
.LBB0_1808:
	s_or_b64 exec, exec, s[6:7]
	s_waitcnt vmcnt(0) lgkmcnt(0)
	s_mov_b32 s60, s96
	s_mov_b32 s61, s97
	s_mov_b64 s[66:67], s[98:99]
	s_mov_b64 s[68:69], s[96:97]
	s_mov_b64 s[70:71], s[98:99]
	s_movk_i32 s72, 0x1000
	s_movk_i32 s73, 0x3fff
	s_movk_i32 s74, 0x2000
	s_movk_i32 s75, 0x3000
	s_mov_b32 s76, 0xf800000
	s_mov_b32 s77, 0x8080808
	s_mov_b32 s78, 0x400000
	s_mov_b32 s79, 0x800000
	s_mov_b32 s80, 0xc00000
	s_mov_b32 s81, 0x1000000
	v_cmp_eq_u32_e64 s[82:83], 0, v1
	s_mov_b64 s[86:87], exec
	v_mul_f32_e32 v202, v207, v207
	v_mul_f32_e32 v203, v209, v209
	v_max_f32_e64 v204, |v207|, |v207|
	v_max_f32_e64 v205, |v206|, |v206|
	v_max_f32_e64 v214, |v209|, |v209|
	v_max_f32_e64 v215, |v208|, |v208|
	s_nop 0
	v_mul_f32_e32 v216, v191, v191
	v_mul_f32_e32 v217, v193, v193
	s_nop 0
	v_mul_f32_e32 v229, v187, v187
	v_mul_f32_e32 v235, v189, v189
	v_fmac_f32_e32 v202, v206, v206
	v_fmac_f32_e32 v203, v208, v208
	v_max_f32_e32 v204, v205, v204
	v_max_f32_e32 v205, v215, v214
	v_fmac_f32_e32 v216, v190, v190
	v_fmac_f32_e32 v217, v192, v192
	v_max_f32_e64 v218, |v191|, |v191|
	v_max_f32_e64 v219, |v190|, |v190|
	v_max_f32_e64 v236, |v187|, |v187|
	v_max_f32_e64 v237, |v186|, |v186|
	s_nop 0
	v_mul_f32_e32 v240, v179, v179
	v_mul_f32_e32 v241, v181, v181
	v_fmac_f32_e32 v229, v186, v186
	v_fmac_f32_e32 v235, v188, v188
	v_add_f32_e32 v202, v202, v203
	v_max3_f32 v203, v204, 0, v205
	v_add_f32_e32 v204, v216, v217
	v_max_f32_e32 v214, v219, v218
	v_max_f32_e32 v218, v237, v236
	v_fmac_f32_e32 v240, v178, v178
	v_fmac_f32_e32 v241, v180, v180
	s_nop 0
	v_mul_f32_e32 v236, v183, v183
	v_mul_f32_e32 v237, v185, v185
	v_add_f32_e32 v205, v229, v235
	v_add_f32_e32 v202, v202, v204
	v_max_f32_e64 v220, |v193|, |v193|
	v_max_f32_e64 v221, |v192|, |v192|
	v_add_f32_e32 v216, v240, v241
	v_fmac_f32_e32 v236, v182, v182
	v_fmac_f32_e32 v237, v184, v184
	v_add_f32_e32 v202, v202, v205
	v_max_f32_e64 v238, |v189|, |v189|
	v_max_f32_e64 v239, |v188|, |v188|
	v_max_f32_e32 v215, v221, v220
	v_add_f32_e32 v202, v202, v216
	v_add_f32_e32 v204, v236, v237
	v_max_f32_e64 v242, |v179|, |v179|
	v_max_f32_e64 v243, |v178|, |v178|
	v_max_f32_e64 v244, |v181|, |v181|
	v_max_f32_e64 v245, |v180|, |v180|
	v_max_f32_e32 v219, v239, v238
	v_max3_f32 v203, v203, v214, v215
	v_add_f32_e32 v202, v202, v204
	v_max_f32_e64 v204, |v183|, |v183|
	v_max_f32_e64 v205, |v182|, |v182|
	v_max_f32_e32 v220, v243, v242
	v_max_f32_e32 v221, v245, v244
	v_max3_f32 v203, v203, v218, v219
	v_max_f32_e32 v204, v205, v204
	v_max_f32_e64 v205, |v185|, |v185|
	v_max_f32_e64 v214, |v184|, |v184|
	v_max3_f32 v203, v203, v220, v221
	v_max_f32_e32 v205, v214, v205
	v_max3_f32 v203, v203, v204, v205
	v_mov_b32_e32 v218, v86
	v_mov_b32_e32 v219, v87
	v_mov_b32_e32 v220, v88
	v_mov_b32_e32 v221, v89
	v_mov_b32_e32 v214, v90
	v_mov_b32_e32 v215, v91
	v_mov_b32_e32 v216, v92
	v_mov_b32_e32 v217, v93
	v_cmp_lt_i32_e32 vcc, v157, v154
	s_nop 0
	v_mul_f32_e32 v204, v171, v171
	v_mul_f32_e32 v194, v173, v173
	v_fmac_f32_e32 v204, v170, v170
	v_fmac_f32_e32 v194, v172, v172
	v_add_f32_e32 v194, v204, v194
	v_add_f32_e32 v194, v202, v194
	v_max_f32_e64 v195, |v171|, |v171|
	v_max_f32_e64 v202, |v170|, |v170|
	v_max_f32_e32 v195, v202, v195
	v_max_f32_e64 v202, |v173|, |v173|
	v_max_f32_e64 v204, |v172|, |v172|
	v_max_f32_e32 v202, v204, v202
	v_max3_f32 v195, v203, v195, v202
	s_nop 0
	v_mul_f32_e32 v202, v223, v223
	v_mul_f32_e32 v203, v225, v225
	v_fmac_f32_e32 v202, v222, v222
	v_fmac_f32_e32 v203, v224, v224
	v_add_f32_e32 v202, v202, v203
	v_add_f32_e32 v194, v194, v202
	v_max_f32_e64 v202, |v223|, |v223|
	v_max_f32_e64 v203, |v222|, |v222|
	v_max_f32_e32 v202, v203, v202
	v_max_f32_e64 v203, |v225|, |v225|
	v_max_f32_e64 v204, |v224|, |v224|
	v_max_f32_e32 v203, v204, v203
	v_max3_f32 v229, v195, v202, v203
	v_mov_b32_e32 v202, v94
	v_mov_b32_e32 v203, v95
	v_mov_b32_e32 v204, v96
	v_mov_b32_e32 v205, v97
	s_nop 0
	v_mul_f32_e32 v195, v211, v211
	v_mul_f32_e32 v235, v213, v213
	v_fmac_f32_e32 v195, v210, v210
	v_fmac_f32_e32 v235, v212, v212
	v_add_f32_e32 v195, v195, v235
	v_add_f32_e32 v235, v194, v195
	v_max_f32_e64 v194, |v211|, |v211|
	v_max_f32_e64 v195, |v210|, |v210|
	v_max_f32_e32 v236, v195, v194
	v_max_f32_e64 v194, |v213|, |v213|
	v_max_f32_e64 v195, |v212|, |v212|
	v_max_f32_e32 v237, v195, v194
	v_mov_b32_e32 v194, v98
	v_mov_b32_e32 v195, v99
	v_mov_b32_e32 v196, v100
	v_mov_b32_e32 v197, v101
	v_max3_f32 v229, v229, v236, v237
	s_nop 0
	v_mul_f32_e32 v236, v199, v199
	v_mul_f32_e32 v237, v201, v201
	v_fmac_f32_e32 v236, v198, v198
	v_fmac_f32_e32 v237, v200, v200
	v_add_f32_e32 v236, v236, v237
	v_add_f32_e32 v235, v235, v236
	v_max_f32_e64 v236, |v199|, |v199|
	v_max_f32_e64 v237, |v198|, |v198|
	v_max_f32_e32 v236, v237, v236
	v_max_f32_e64 v237, |v201|, |v201|
	v_max_f32_e64 v238, |v200|, |v200|
	v_max_f32_e32 v237, v238, v237
	v_max3_f32 v229, v229, v236, v237
	s_nop 0
	v_mul_f32_e32 v236, v175, v175
	v_mul_f32_e32 v237, v177, v177
	v_fmac_f32_e32 v236, v174, v174
	v_fmac_f32_e32 v237, v176, v176
	v_add_f32_e32 v236, v236, v237
	v_add_f32_e32 v235, v235, v236
	v_max_f32_e64 v236, |v175|, |v175|
	v_max_f32_e64 v237, |v174|, |v174|
	v_max_f32_e32 v236, v237, v236
	v_max_f32_e64 v237, |v177|, |v177|
	v_max_f32_e64 v238, |v176|, |v176|
	v_max_f32_e32 v237, v238, v237
	v_max3_f32 v229, v229, v236, v237
	s_nop 0
	v_mul_f32_e32 v236, v167, v167
	v_mul_f32_e32 v237, v169, v169
	v_fmac_f32_e32 v236, v166, v166
	v_fmac_f32_e32 v237, v168, v168
	v_add_f32_e32 v236, v236, v237
	v_add_f32_e32 v235, v235, v236
	v_max_f32_e64 v236, |v167|, |v167|
	v_max_f32_e64 v237, |v166|, |v166|
	v_max_f32_e32 v236, v237, v236
	v_max_f32_e64 v237, |v169|, |v169|
	v_max_f32_e64 v238, |v168|, |v168|
	v_max_f32_e32 v237, v238, v237
	v_max3_f32 v229, v229, v236, v237
	s_nop 0
	v_mul_f32_e32 v236, v219, v219
	v_mul_f32_e32 v237, v221, v221
	v_fmac_f32_e32 v236, v218, v218
	v_fmac_f32_e32 v237, v220, v220
	v_add_f32_e32 v236, v236, v237
	v_add_f32_e32 v235, v235, v236
	v_max_f32_e64 v236, |v219|, |v219|
	v_max_f32_e64 v237, |v218|, |v218|
	v_max_f32_e32 v236, v237, v236
	v_max_f32_e64 v237, |v221|, |v221|
	v_max_f32_e64 v238, |v220|, |v220|
	v_max_f32_e32 v237, v238, v237
	v_max3_f32 v229, v229, v236, v237
	s_nop 0
	v_mul_f32_e32 v236, v215, v215
	v_mul_f32_e32 v237, v217, v217
	v_fmac_f32_e32 v236, v214, v214
	v_fmac_f32_e32 v237, v216, v216
	v_add_f32_e32 v236, v236, v237
	v_add_f32_e32 v235, v235, v236
	v_max_f32_e64 v236, |v215|, |v215|
	v_max_f32_e64 v237, |v214|, |v214|
	v_max_f32_e32 v236, v237, v236
	v_max_f32_e64 v237, |v217|, |v217|
	v_max_f32_e64 v238, |v216|, |v216|
	v_max_f32_e32 v237, v238, v237
	v_max3_f32 v229, v229, v236, v237
	s_nop 0
	v_mul_f32_e32 v236, v203, v203
	v_mul_f32_e32 v237, v205, v205
	v_fmac_f32_e32 v236, v202, v202
	v_fmac_f32_e32 v237, v204, v204
	v_add_f32_e32 v236, v236, v237
	v_add_f32_e32 v235, v235, v236
	v_max_f32_e64 v236, |v203|, |v203|
	v_max_f32_e64 v237, |v202|, |v202|
	v_max_f32_e32 v236, v237, v236
	v_max_f32_e64 v237, |v205|, |v205|
	v_max_f32_e64 v238, |v204|, |v204|
	v_max_f32_e32 v237, v238, v237
	v_max3_f32 v229, v229, v236, v237
	s_nop 0
	v_mul_f32_e32 v236, v195, v195
	v_mul_f32_e32 v237, v197, v197
	v_fmac_f32_e32 v236, v194, v194
	v_fmac_f32_e32 v237, v196, v196
	v_add_f32_e32 v236, v236, v237
	v_add_f32_e32 v235, v235, v236
	v_max_f32_e64 v236, |v195|, |v195|
	v_max_f32_e64 v237, |v194|, |v194|
	v_max_f32_e32 v236, v237, v236
	v_max_f32_e64 v237, |v197|, |v197|
	v_max_f32_e64 v238, |v196|, |v196|
	v_max_f32_e32 v237, v238, v237
	v_max3_f32 v229, v229, v236, v237
	v_mul_f32_e32 v236, v163, v163
	v_mul_f32_e32 v237, v165, v165
	v_fmac_f32_e32 v236, v162, v162
	v_fmac_f32_e32 v237, v164, v164
	v_add_f32_e32 v236, v236, v237
	v_add_f32_e32 v235, v235, v236
	v_max_f32_e64 v236, |v163|, |v163|
	v_max_f32_e64 v237, |v162|, |v162|
	v_max_f32_e32 v236, v237, v236
	v_max_f32_e64 v237, |v165|, |v165|
	v_max_f32_e64 v240, |v164|, |v164|
	v_cndmask_b32_e32 v238, v1, v157, vcc
	v_max_f32_e32 v237, v240, v237
	v_lshlrev_b32_e32 v238, 2, v238
	v_max3_f32 v229, v229, v236, v237
	ds_bpermute_b32 v239, v238, v235
	ds_bpermute_b32 v236, v238, v229
	v_cmp_lt_i32_e32 vcc, v158, v154
	s_waitcnt lgkmcnt(1)
	v_add_f32_e32 v235, v235, v239
	v_cndmask_b32_e32 v237, v1, v158, vcc
	v_lshlrev_b32_e32 v237, 2, v237
	s_waitcnt lgkmcnt(0)
	v_max_f32_e32 v236, v236, v236
	ds_bpermute_b32 v238, v237, v235
	v_max_f32_e32 v229, v229, v236
	ds_bpermute_b32 v236, v237, v229
	v_cmp_lt_i32_e32 vcc, v159, v154
	s_waitcnt lgkmcnt(1)
	v_add_f32_e32 v235, v235, v238
	v_cndmask_b32_e32 v237, v1, v159, vcc
	v_lshlrev_b32_e32 v237, 2, v237
	ds_bpermute_b32 v238, v237, v235
	s_waitcnt lgkmcnt(1)
	v_max_f32_e32 v236, v236, v236
	v_max_f32_e32 v229, v229, v236
	ds_bpermute_b32 v236, v237, v229
	v_cmp_lt_i32_e32 vcc, v160, v154
	s_waitcnt lgkmcnt(1)
	v_add_f32_e32 v235, v235, v238
	s_waitcnt lgkmcnt(0)
	v_max_f32_e32 v236, v236, v236
	v_cndmask_b32_e32 v237, v1, v160, vcc
	v_lshlrev_b32_e32 v237, 2, v237
	ds_bpermute_b32 v238, v237, v235
	v_max_f32_e32 v229, v229, v236
	ds_bpermute_b32 v236, v237, v229
	v_cmp_lt_i32_e32 vcc, v156, v154
	s_waitcnt lgkmcnt(1)
	v_add_f32_e32 v235, v235, v238
	v_cndmask_b32_e32 v237, v1, v156, vcc
	v_lshlrev_b32_e32 v237, 2, v237
	ds_bpermute_b32 v238, v237, v235
	s_waitcnt lgkmcnt(1)
	v_max_f32_e32 v236, v236, v236
	v_max_f32_e32 v229, v229, v236
	v_cmp_lt_i32_e32 vcc, v155, v154
	ds_bpermute_b32 v236, v237, v229
	s_waitcnt lgkmcnt(1)
	v_add_f32_e32 v235, v235, v238
	v_cndmask_b32_e32 v237, v1, v155, vcc
	v_lshlrev_b32_e32 v237, 2, v237
	ds_bpermute_b32 v238, v237, v235
	s_waitcnt lgkmcnt(1)
	v_max_f32_e32 v236, v236, v236
	v_max_f32_e32 v229, v229, v236
	ds_bpermute_b32 v236, v237, v229
	s_waitcnt lgkmcnt(1)
	v_add_f32_e32 v235, v235, v238
	v_mul_f32_e32 v235, 0x39800000, v235
	v_mul_f32_e32 v237, 0x4f800000, v235
	v_cmp_gt_f32_e32 vcc, s76, v235
	s_waitcnt lgkmcnt(0)
	v_max_f32_e32 v236, v236, v236
	v_max_f32_e32 v229, v229, v236
	v_cndmask_b32_e32 v235, v235, v237, vcc
	v_sqrt_f32_e32 v237, v235
	v_mul_f32_e32 v229, 0x3e088889, v229
	v_add_u32_e32 v236, -1, v237
	v_fma_f32 v238, -v236, v237, v235
	v_cmp_ge_f32_e64 s[88:89], 0, v238
	v_add_u32_e32 v238, 1, v237
	s_nop 0
	v_cndmask_b32_e64 v236, v237, v236, s[88:89]
	v_fma_f32 v237, -v238, v237, v235
	v_cmp_lt_f32_e64 s[88:89], 0, v237
	s_nop 1
	v_cndmask_b32_e64 v236, v236, v238, s[88:89]
	v_mul_f32_e32 v237, 0x37800000, v236
	v_cndmask_b32_e32 v236, v236, v237, vcc
	v_cmp_class_f32_e32 vcc, v235, v233
	s_nop 1
	v_cndmask_b32_e32 v235, v236, v235, vcc
	v_mul_f32_e32 v235, 0x3eab9f56, v235
	v_min_f32_e32 v229, v235, v229
	v_max_f32_e32 v235, 0xda24260, v229
	v_div_scale_f32 v229, s[88:89], v235, v235, 1.0
	v_rcp_f32_e32 v236, v229
	s_nop 0
	v_fma_f32 v237, -v229, v236, 1.0
	v_fmac_f32_e32 v236, v237, v236
	v_div_scale_f32 v237, vcc, 1.0, v235, 1.0
	v_mul_f32_e32 v238, v237, v236
	v_fma_f32 v239, -v229, v238, v237
	v_fmac_f32_e32 v238, v239, v236
	v_fma_f32 v229, -v229, v238, v237
	v_div_fmas_f32 v229, v229, v236, v238
	v_div_fixup_f32 v229, v229, v235, 1.0
	v_mul_f32_e32 v179, v179, v229
	v_mul_f32_e32 v178, v178, v229
	v_floor_f32_e32 v179, v179
	v_mul_f32_e32 v180, v180, v229
	v_floor_f32_e32 v178, v178
	v_add_f32_e32 v179, 0x41000000, v179
	v_floor_f32_e32 v180, v180
	v_add_f32_e32 v178, 0x41000000, v178
	v_med3_f32 v179, v179, 0, v234
	v_add_f32_e32 v180, 0x41000000, v180
	v_med3_f32 v178, v178, 0, v234
	v_cvt_i32_f32_e32 v179, v179
	v_med3_f32 v180, v180, 0, v234
	v_cvt_i32_f32_e32 v178, v178
	v_cvt_i32_f32_sdwa v180, v180 dst_sel:WORD_1 dst_unused:UNUSED_PAD src0_sel:DWORD
	v_lshlrev_b32_e32 v179, 8, v179
	v_mul_f32_e32 v171, v171, v229
	v_mul_f32_e32 v170, v170, v229
	v_or3_b32 v178, v179, v178, v180
	v_mul_f32_e32 v179, v181, v229
	v_mul_f32_e32 v181, v183, v229
	v_floor_f32_e32 v179, v179
	v_mul_f32_e32 v180, v182, v229
	v_floor_f32_e32 v181, v181
	v_mul_f32_e32 v182, v184, v229
	v_add_f32_e32 v179, 0x41000000, v179
	v_floor_f32_e32 v180, v180
	v_add_f32_e32 v181, 0x41000000, v181
	v_floor_f32_e32 v182, v182
	v_mul_f32_e32 v183, v185, v229
	v_floor_f32_e32 v171, v171
	v_mul_f32_e32 v172, v172, v229
	v_med3_f32 v179, v179, 0, v234
	v_add_f32_e32 v180, 0x41000000, v180
	v_med3_f32 v181, v181, 0, v234
	v_add_f32_e32 v182, 0x41000000, v182
	v_floor_f32_e32 v183, v183
	v_floor_f32_e32 v170, v170
	v_add_f32_e32 v171, 0x41000000, v171
	v_floor_f32_e32 v172, v172
	v_mul_f32_e32 v175, v175, v229
	v_cvt_i32_f32_sdwa v179, v179 dst_sel:BYTE_3 dst_unused:UNUSED_PAD src0_sel:DWORD
	v_med3_f32 v180, v180, 0, v234
	v_cvt_i32_f32_e32 v181, v181
	v_med3_f32 v182, v182, 0, v234
	v_add_f32_e32 v183, 0x41000000, v183
	v_add_f32_e32 v170, 0x41000000, v170
	v_med3_f32 v171, v171, 0, v234
	v_add_f32_e32 v172, 0x41000000, v172
	v_mul_f32_e32 v174, v174, v229
	v_floor_f32_e32 v175, v175
	v_mul_f32_e32 v176, v176, v229
	v_cvt_i32_f32_e32 v180, v180
	v_cvt_i32_f32_sdwa v182, v182 dst_sel:WORD_1 dst_unused:UNUSED_PAD src0_sel:DWORD
	v_med3_f32 v183, v183, 0, v234
	v_med3_f32 v170, v170, 0, v234
	v_cvt_i32_f32_e32 v171, v171
	v_med3_f32 v172, v172, 0, v234
	v_floor_f32_e32 v174, v174
	v_add_f32_e32 v175, 0x41000000, v175
	v_floor_f32_e32 v176, v176
	v_cvt_i32_f32_sdwa v183, v183 dst_sel:BYTE_3 dst_unused:UNUSED_PAD src0_sel:DWORD
	v_cvt_i32_f32_e32 v170, v170
	v_cvt_i32_f32_sdwa v172, v172 dst_sel:WORD_1 dst_unused:UNUSED_PAD src0_sel:DWORD
	v_add_f32_e32 v174, 0x41000000, v174
	v_med3_f32 v175, v175, 0, v234
	v_add_f32_e32 v176, 0x41000000, v176
	v_med3_f32 v174, v174, 0, v234
	v_cvt_i32_f32_e32 v175, v175
	v_med3_f32 v176, v176, 0, v234
	v_bitop3_b32 v178, v178, s77, v179 bitop3:0x36
	v_lshlrev_b32_e32 v179, 8, v181
	v_cvt_i32_f32_e32 v174, v174
	v_cvt_i32_f32_sdwa v176, v176 dst_sel:WORD_1 dst_unused:UNUSED_PAD src0_sel:DWORD
	v_or3_b32 v179, v179, v180, v182
	v_lshlrev_b32_e32 v171, 8, v171
	v_or_b32_e32 v180, v179, v183
	v_bitop3_b32 v179, v179, s77, v183 bitop3:0x36
	v_or3_b32 v170, v171, v170, v172
	v_mul_f32_e32 v171, v173, v229
	v_mul_f32_e32 v173, v223, v229
	v_cndmask_b32_e64 v179, v179, v180, s[86:87]
	v_floor_f32_e32 v171, v171
	v_mul_f32_e32 v172, v222, v229
	v_floor_f32_e32 v173, v173
	v_mul_f32_e32 v180, v224, v229
	v_lshlrev_b32_e32 v175, 8, v175
	v_add_f32_e32 v171, 0x41000000, v171
	v_floor_f32_e32 v172, v172
	v_add_f32_e32 v173, 0x41000000, v173
	v_floor_f32_e32 v180, v180
	v_or3_b32 v174, v175, v174, v176
	v_mul_f32_e32 v175, v177, v229
	v_mul_f32_e32 v167, v167, v229
	v_med3_f32 v171, v171, 0, v234
	v_add_f32_e32 v172, 0x41000000, v172
	v_med3_f32 v173, v173, 0, v234
	v_add_f32_e32 v180, 0x41000000, v180
	v_floor_f32_e32 v175, v175
	v_mul_f32_e32 v166, v166, v229
	v_floor_f32_e32 v167, v167
	v_mul_f32_e32 v168, v168, v229
	v_cvt_i32_f32_sdwa v171, v171 dst_sel:BYTE_3 dst_unused:UNUSED_PAD src0_sel:DWORD
	v_med3_f32 v172, v172, 0, v234
	v_cvt_i32_f32_e32 v173, v173
	v_med3_f32 v180, v180, 0, v234
	v_add_f32_e32 v175, 0x41000000, v175
	v_floor_f32_e32 v166, v166
	v_add_f32_e32 v167, 0x41000000, v167
	v_floor_f32_e32 v168, v168
	v_cvt_i32_f32_e32 v172, v172
	v_cvt_i32_f32_sdwa v180, v180 dst_sel:WORD_1 dst_unused:UNUSED_PAD src0_sel:DWORD
	v_med3_f32 v175, v175, 0, v234
	v_add_f32_e32 v166, 0x41000000, v166
	v_med3_f32 v167, v167, 0, v234
	v_add_f32_e32 v168, 0x41000000, v168
	v_cvt_i32_f32_sdwa v175, v175 dst_sel:BYTE_3 dst_unused:UNUSED_PAD src0_sel:DWORD
	v_med3_f32 v166, v166, 0, v234
	v_cvt_i32_f32_e32 v167, v167
	v_med3_f32 v168, v168, 0, v234
	v_cvt_i32_f32_e32 v166, v166
	v_cvt_i32_f32_sdwa v168, v168 dst_sel:WORD_1 dst_unused:UNUSED_PAD src0_sel:DWORD
	v_mul_f32_e32 v181, v225, v229
	v_bitop3_b32 v170, v170, s77, v171 bitop3:0x36
	v_lshlrev_b32_e32 v171, 8, v173
	v_floor_f32_e32 v181, v181
	v_or3_b32 v171, v171, v172, v180
	v_mul_f32_e32 v180, v211, v229
	v_mul_f32_e32 v169, v169, v229
	v_add_f32_e32 v181, 0x41000000, v181
	v_mul_f32_e32 v173, v210, v229
	v_floor_f32_e32 v180, v180
	v_mul_f32_e32 v182, v212, v229
	v_floor_f32_e32 v169, v169
	v_bitop3_b32 v174, v174, s77, v175 bitop3:0x36
	v_lshlrev_b32_e32 v167, 8, v167
	v_mul_f32_e32 v175, v219, v229
	v_med3_f32 v181, v181, 0, v234
	v_floor_f32_e32 v173, v173
	v_add_f32_e32 v180, 0x41000000, v180
	v_floor_f32_e32 v182, v182
	v_add_f32_e32 v169, 0x41000000, v169
	v_or3_b32 v166, v167, v166, v168
	v_mul_f32_e32 v168, v218, v229
	v_floor_f32_e32 v175, v175
	v_mul_f32_e32 v176, v220, v229
	v_cvt_i32_f32_sdwa v181, v181 dst_sel:BYTE_3 dst_unused:UNUSED_PAD src0_sel:DWORD
	v_add_f32_e32 v173, 0x41000000, v173
	v_med3_f32 v180, v180, 0, v234
	v_add_f32_e32 v182, 0x41000000, v182
	v_med3_f32 v169, v169, 0, v234
	v_floor_f32_e32 v168, v168
	v_add_f32_e32 v175, 0x41000000, v175
	v_floor_f32_e32 v176, v176
	v_med3_f32 v173, v173, 0, v234
	v_cvt_i32_f32_e32 v180, v180
	v_med3_f32 v182, v182, 0, v234
	v_cvt_i32_f32_sdwa v169, v169 dst_sel:BYTE_3 dst_unused:UNUSED_PAD src0_sel:DWORD
	v_add_f32_e32 v168, 0x41000000, v168
	v_med3_f32 v175, v175, 0, v234
	v_add_f32_e32 v176, 0x41000000, v176
	v_cvt_i32_f32_e32 v173, v173
	v_cvt_i32_f32_sdwa v182, v182 dst_sel:WORD_1 dst_unused:UNUSED_PAD src0_sel:DWORD
	v_med3_f32 v168, v168, 0, v234
	v_cvt_i32_f32_e32 v175, v175
	v_med3_f32 v176, v176, 0, v234
	v_cvt_i32_f32_e32 v168, v168
	v_cvt_i32_f32_sdwa v176, v176 dst_sel:WORD_1 dst_unused:UNUSED_PAD src0_sel:DWORD
	v_or_b32_e32 v172, v171, v181
	v_bitop3_b32 v171, v171, s77, v181 bitop3:0x36
	v_cndmask_b32_e64 v171, v171, v172, s[86:87]
	v_lshlrev_b32_e32 v172, 8, v180
	v_or_b32_e32 v167, v166, v169
	v_bitop3_b32 v166, v166, s77, v169 bitop3:0x36
	v_or3_b32 v172, v172, v173, v182
	v_mul_f32_e32 v173, v213, v229
	v_mul_f32_e32 v181, v199, v229
	v_cndmask_b32_e64 v166, v166, v167, s[86:87]
	v_lshlrev_b32_e32 v167, 8, v175
	v_floor_f32_e32 v173, v173
	v_mul_f32_e32 v180, v198, v229
	v_floor_f32_e32 v181, v181
	v_mul_f32_e32 v182, v200, v229
	v_or3_b32 v167, v167, v168, v176
	v_mul_f32_e32 v168, v221, v229
	v_mul_f32_e32 v175, v215, v229
	v_add_f32_e32 v173, 0x41000000, v173
	v_floor_f32_e32 v180, v180
	v_add_f32_e32 v181, 0x41000000, v181
	v_floor_f32_e32 v182, v182
	v_mul_f32_e32 v183, v201, v229
	v_floor_f32_e32 v168, v168
	v_mul_f32_e32 v169, v214, v229
	v_floor_f32_e32 v175, v175
	v_mul_f32_e32 v176, v216, v229
	v_med3_f32 v173, v173, 0, v234
	v_add_f32_e32 v180, 0x41000000, v180
	v_med3_f32 v181, v181, 0, v234
	v_add_f32_e32 v182, 0x41000000, v182
	v_floor_f32_e32 v183, v183
	v_add_f32_e32 v168, 0x41000000, v168
	v_floor_f32_e32 v169, v169
	v_add_f32_e32 v175, 0x41000000, v175
	v_floor_f32_e32 v176, v176
	v_cvt_i32_f32_sdwa v173, v173 dst_sel:BYTE_3 dst_unused:UNUSED_PAD src0_sel:DWORD
	v_med3_f32 v180, v180, 0, v234
	v_cvt_i32_f32_e32 v181, v181
	v_med3_f32 v182, v182, 0, v234
	v_add_f32_e32 v183, 0x41000000, v183
	v_med3_f32 v168, v168, 0, v234
	v_add_f32_e32 v169, 0x41000000, v169
	v_med3_f32 v175, v175, 0, v234
	v_add_f32_e32 v176, 0x41000000, v176
	v_cvt_i32_f32_e32 v180, v180
	v_cvt_i32_f32_sdwa v182, v182 dst_sel:WORD_1 dst_unused:UNUSED_PAD src0_sel:DWORD
	v_med3_f32 v183, v183, 0, v234
	v_cvt_i32_f32_sdwa v168, v168 dst_sel:BYTE_3 dst_unused:UNUSED_PAD src0_sel:DWORD
	v_med3_f32 v169, v169, 0, v234
	v_cvt_i32_f32_e32 v175, v175
	v_med3_f32 v176, v176, 0, v234
	v_cvt_i32_f32_sdwa v183, v183 dst_sel:BYTE_3 dst_unused:UNUSED_PAD src0_sel:DWORD
	v_cvt_i32_f32_e32 v169, v169
	v_cvt_i32_f32_sdwa v176, v176 dst_sel:WORD_1 dst_unused:UNUSED_PAD src0_sel:DWORD
	v_bitop3_b32 v172, v172, s77, v173 bitop3:0x36
	v_lshlrev_b32_e32 v173, 8, v181
	v_or3_b32 v173, v173, v180, v182
	v_mul_f32_e32 v177, v217, v229
	v_bitop3_b32 v167, v167, s77, v168 bitop3:0x36
	v_lshlrev_b32_e32 v168, 8, v175
	v_or_b32_e32 v180, v173, v183
	v_bitop3_b32 v173, v173, s77, v183 bitop3:0x36
	v_floor_f32_e32 v177, v177
	v_or3_b32 v168, v168, v169, v176
	v_mul_f32_e32 v176, v203, v229
	v_cndmask_b32_e64 v173, v173, v180, s[86:87]
	v_add_f32_e32 v177, 0x41000000, v177
	v_mul_f32_e32 v175, v202, v229
	v_floor_f32_e32 v176, v176
	v_mul_f32_e32 v180, v204, v229
	v_med3_f32 v177, v177, 0, v234
	v_floor_f32_e32 v175, v175
	v_add_f32_e32 v176, 0x41000000, v176
	v_floor_f32_e32 v180, v180
	v_cvt_i32_f32_sdwa v177, v177 dst_sel:BYTE_3 dst_unused:UNUSED_PAD src0_sel:DWORD
	v_add_f32_e32 v175, 0x41000000, v175
	v_med3_f32 v176, v176, 0, v234
	v_add_f32_e32 v180, 0x41000000, v180
	v_med3_f32 v175, v175, 0, v234
	v_cvt_i32_f32_e32 v176, v176
	v_med3_f32 v180, v180, 0, v234
	v_cvt_i32_f32_e32 v175, v175
	v_cvt_i32_f32_sdwa v180, v180 dst_sel:WORD_1 dst_unused:UNUSED_PAD src0_sel:DWORD
	v_mul_f32_e32 v191, v191, v229
	v_mul_f32_e32 v190, v190, v229
	v_floor_f32_e32 v191, v191
	v_mul_f32_e32 v192, v192, v229
	v_or_b32_e32 v169, v168, v177
	v_bitop3_b32 v168, v168, s77, v177 bitop3:0x36
	v_floor_f32_e32 v190, v190
	v_add_f32_e32 v191, 0x41000000, v191
	v_floor_f32_e32 v192, v192
	v_cndmask_b32_e64 v168, v168, v169, s[86:87]
	v_lshlrev_b32_e32 v169, 8, v176
	v_add_f32_e32 v190, 0x41000000, v190
	v_med3_f32 v191, v191, 0, v234
	v_add_f32_e32 v192, 0x41000000, v192
	v_or3_b32 v169, v169, v175, v180
	v_mul_f32_e32 v175, v205, v229
	v_mul_f32_e32 v177, v195, v229
	v_med3_f32 v190, v190, 0, v234
	v_cvt_i32_f32_e32 v191, v191
	v_med3_f32 v192, v192, 0, v234
	v_floor_f32_e32 v175, v175
	v_mul_f32_e32 v176, v194, v229
	v_floor_f32_e32 v177, v177
	v_mul_f32_e32 v180, v196, v229
	v_mul_f32_e32 v163, v163, v229
	v_cvt_i32_f32_e32 v190, v190
	v_cvt_i32_f32_sdwa v192, v192 dst_sel:WORD_1 dst_unused:UNUSED_PAD src0_sel:DWORD
	v_add_f32_e32 v175, 0x41000000, v175
	v_floor_f32_e32 v176, v176
	v_add_f32_e32 v177, 0x41000000, v177
	v_floor_f32_e32 v180, v180
	v_mul_f32_e32 v181, v197, v229
	v_mul_f32_e32 v162, v162, v229
	v_floor_f32_e32 v163, v163
	v_mul_f32_e32 v164, v164, v229
	v_mul_f32_e32 v207, v207, v229
	v_med3_f32 v175, v175, 0, v234
	v_add_f32_e32 v176, 0x41000000, v176
	v_med3_f32 v177, v177, 0, v234
	v_add_f32_e32 v180, 0x41000000, v180
	v_floor_f32_e32 v181, v181
	v_floor_f32_e32 v162, v162
	v_add_f32_e32 v163, 0x41000000, v163
	v_floor_f32_e32 v164, v164
	v_mul_f32_e32 v165, v165, v229
	v_mul_f32_e32 v206, v206, v229
	v_floor_f32_e32 v207, v207
	v_mul_f32_e32 v208, v208, v229
	v_cvt_i32_f32_sdwa v175, v175 dst_sel:BYTE_3 dst_unused:UNUSED_PAD src0_sel:DWORD
	v_med3_f32 v176, v176, 0, v234
	v_cvt_i32_f32_e32 v177, v177
	v_med3_f32 v180, v180, 0, v234
	v_add_f32_e32 v181, 0x41000000, v181
	v_add_f32_e32 v162, 0x41000000, v162
	v_med3_f32 v163, v163, 0, v234
	v_add_f32_e32 v164, 0x41000000, v164
	v_floor_f32_e32 v165, v165
	v_floor_f32_e32 v206, v206
	v_add_f32_e32 v207, 0x41000000, v207
	v_floor_f32_e32 v208, v208
	v_mul_f32_e32 v209, v209, v229
	v_lshlrev_b32_e32 v191, 8, v191
	v_mul_f32_e32 v187, v187, v229
	v_cvt_i32_f32_e32 v176, v176
	v_cvt_i32_f32_sdwa v180, v180 dst_sel:WORD_1 dst_unused:UNUSED_PAD src0_sel:DWORD
	v_med3_f32 v181, v181, 0, v234
	v_med3_f32 v162, v162, 0, v234
	v_cvt_i32_f32_e32 v163, v163
	v_med3_f32 v164, v164, 0, v234
	v_add_f32_e32 v165, 0x41000000, v165
	v_add_f32_e32 v206, 0x41000000, v206
	v_med3_f32 v207, v207, 0, v234
	v_add_f32_e32 v208, 0x41000000, v208
	v_floor_f32_e32 v209, v209
	v_or3_b32 v190, v191, v190, v192
	v_mul_f32_e32 v191, v193, v229
	v_mul_f32_e32 v186, v186, v229
	v_floor_f32_e32 v187, v187
	v_mul_f32_e32 v188, v188, v229
	v_cvt_i32_f32_sdwa v181, v181 dst_sel:BYTE_3 dst_unused:UNUSED_PAD src0_sel:DWORD
	v_cvt_i32_f32_e32 v162, v162
	v_cvt_i32_f32_sdwa v164, v164 dst_sel:WORD_1 dst_unused:UNUSED_PAD src0_sel:DWORD
	v_med3_f32 v165, v165, 0, v234
	v_med3_f32 v206, v206, 0, v234
	v_cvt_i32_f32_e32 v207, v207
	v_med3_f32 v208, v208, 0, v234
	v_add_f32_e32 v209, 0x41000000, v209
	v_floor_f32_e32 v191, v191
	v_floor_f32_e32 v186, v186
	v_add_f32_e32 v187, 0x41000000, v187
	v_floor_f32_e32 v188, v188
	v_mul_f32_e32 v189, v189, v229
	v_cvt_i32_f32_sdwa v165, v165 dst_sel:BYTE_3 dst_unused:UNUSED_PAD src0_sel:DWORD
	v_cvt_i32_f32_e32 v206, v206
	v_cvt_i32_f32_sdwa v208, v208 dst_sel:WORD_1 dst_unused:UNUSED_PAD src0_sel:DWORD
	v_med3_f32 v209, v209, 0, v234
	v_add_f32_e32 v191, 0x41000000, v191
	v_add_f32_e32 v186, 0x41000000, v186
	v_med3_f32 v187, v187, 0, v234
	v_add_f32_e32 v188, 0x41000000, v188
	v_floor_f32_e32 v189, v189
	v_bitop3_b32 v169, v169, s77, v175 bitop3:0x36
	v_lshlrev_b32_e32 v175, 8, v177
	v_cvt_i32_f32_sdwa v209, v209 dst_sel:BYTE_3 dst_unused:UNUSED_PAD src0_sel:DWORD
	v_med3_f32 v191, v191, 0, v234
	v_med3_f32 v186, v186, 0, v234
	v_cvt_i32_f32_e32 v187, v187
	v_med3_f32 v188, v188, 0, v234
	v_add_f32_e32 v189, 0x41000000, v189
	v_or3_b32 v175, v175, v176, v180
	v_lshlrev_b32_e32 v163, 8, v163
	v_cvt_i32_f32_sdwa v191, v191 dst_sel:BYTE_3 dst_unused:UNUSED_PAD src0_sel:DWORD
	v_cvt_i32_f32_e32 v186, v186
	v_cvt_i32_f32_sdwa v188, v188 dst_sel:WORD_1 dst_unused:UNUSED_PAD src0_sel:DWORD
	v_med3_f32 v189, v189, 0, v234
	v_or_b32_e32 v176, v175, v181
	v_bitop3_b32 v175, v175, s77, v181 bitop3:0x36
	v_or3_b32 v162, v163, v162, v164
	v_lshlrev_b32_e32 v207, 8, v207
	v_cvt_i32_f32_sdwa v189, v189 dst_sel:BYTE_3 dst_unused:UNUSED_PAD src0_sel:DWORD
	v_cndmask_b32_e64 v175, v175, v176, s[86:87]
	v_bitop3_b32 v176, v162, s77, v165 bitop3:0x36
	v_mov_b32_e32 v162, s61
	v_mov_b32_e32 v163, s69
	v_or3_b32 v206, v207, v206, v208
	v_cndmask_b32_e64 v163, v162, v163, s[86:87]
	v_mov_b32_e32 v162, s60
	v_mov_b32_e32 v164, s68
	v_or_b32_e32 v207, v206, v209
	v_bitop3_b32 v206, v206, s77, v209 bitop3:0x36
	v_lshlrev_b32_e32 v187, 8, v187
	v_cndmask_b32_e64 v162, v162, v164, s[86:87]
	v_lshlrev_b64 v[164:165], 8, v[230:231]
	v_cndmask_b32_e64 v206, v206, v207, s[86:87]
	v_bitop3_b32 v190, v190, s77, v191 bitop3:0x36
	v_or3_b32 v186, v187, v186, v188
	v_lshl_add_u64 v[162:163], v[162:163], 0, v[164:165]
	v_mov_b32_e32 v229, v227
	v_or_b32_e32 v187, v186, v189
	v_bitop3_b32 v186, v186, s77, v189 bitop3:0x36
	v_lshl_add_u64 v[162:163], v[162:163], 0, v[228:229]
	v_lshl_or_b32 v164, v190, 4, v206
	v_cndmask_b32_e64 v186, v186, v187, s[86:87]
	global_store_dword v[162:163], v164, off
	v_add_co_u32_e32 v164, vcc, s78, v162
	v_lshl_or_b32 v177, v178, 4, v186
	s_nop 0
	v_addc_co_u32_e32 v165, vcc, 0, v163, vcc
	global_store_dword v[164:165], v177, off
	v_add_co_u32_e32 v164, vcc, s79, v162
	v_lshl_or_b32 v170, v170, 4, v179
	s_nop 0
	v_addc_co_u32_e32 v165, vcc, 0, v163, vcc
	global_store_dword v[164:165], v170, off
	v_add_co_u32_e32 v164, vcc, s80, v162
	v_lshl_or_b32 v170, v172, 4, v171
	s_nop 0
	v_addc_co_u32_e32 v165, vcc, 0, v163, vcc
	global_store_dword v[164:165], v170, off
	v_add_co_u32_e32 v164, vcc, s81, v162
	v_lshl_or_b32 v170, v174, 4, v173
	s_nop 0
	v_addc_co_u32_e32 v165, vcc, 0, v163, vcc
	global_store_dword v[164:165], v170, off
	v_add_co_u32_e32 v164, vcc, 0x1400000, v162
	v_lshl_or_b32 v166, v167, 4, v166
	s_nop 0
	v_addc_co_u32_e32 v165, vcc, 0, v163, vcc
	global_store_dword v[164:165], v166, off
	v_add_co_u32_e32 v164, vcc, 0x1800000, v162
	v_lshl_or_b32 v166, v169, 4, v168
	s_nop 0
	v_addc_co_u32_e32 v165, vcc, 0, v163, vcc
	v_add_co_u32_e32 v162, vcc, 0x1c00000, v162
	global_store_dword v[164:165], v166, off
	v_lshl_or_b32 v164, v176, 4, v175
	v_addc_co_u32_e32 v163, vcc, 0, v163, vcc
	global_store_dword v[162:163], v164, off
	s_and_saveexec_b64 s[88:89], s[82:83]
	s_cbranch_execz .Luvh_skip_scale
	v_mov_b32_e32 v162, s67
	v_mov_b32_e32 v163, s71
	v_cndmask_b32_e64 v163, v162, v163, s[86:87]
	v_mov_b32_e32 v162, s66
	v_mov_b32_e32 v164, s70
	v_cndmask_b32_e64 v162, v162, v164, s[86:87]
	v_lshl_add_u64 v[162:163], v[230:231], 2, v[162:163]
	global_store_dword v[162:163], v235, off
.Luvh_skip_scale:
	s_or_b64 exec, exec, s[88:89]
	s_waitcnt lgkmcnt(0)
	s_add_i32 s47, s47, s53
	s_cmpk_lt_u32 s47, 0x100
	s_cbranch_scc0 .LBB0_1936
.LBB0_1809:
	s_lshl_b32 s56, s47, 5
	v_add_u32_e32 v2, s56, v72
	v_ashrrev_i32_e32 v3, 31, v2
	v_lshlrev_b64 v[2:3], 12, v[2:3]
	v_lshl_add_u64 v[10:11], v[38:39], 0, v[2:3]
	s_waitcnt lgkmcnt(0)
	s_barrier
	global_load_dwordx4 v[2:5], v[10:11], off
	global_load_dwordx4 v[6:9], v[10:11], off offset:16
	s_waitcnt vmcnt(1)
	ds_write_b128 v76, v[2:5]
	s_waitcnt vmcnt(0)
	ds_write_b128 v76, v[6:9] offset:16
	s_lshr_b32 s60, s47, 5
	s_lshl_b32 s61, s2, 3
	s_add_i32 s60, s60, s61
	s_addk_i32 s60, 0x800
	v_mov_b32_e32 v162, s60
	s_mov_b64 s[62:63], s[94:95]
	s_mov_b64 s[64:65], s[94:95]
	s_movk_i32 s72, 0x1000
	s_movk_i32 s73, 0x3fff
	s_movk_i32 s74, 0x2000
	s_movk_i32 s75, 0x3000
	v_lshl_add_u32 v162, v162, 3, v232
	v_add_u32_e32 v163, 0xffffc000, v162
	v_cmp_lt_i32_e64 s[86:87], s73, v162
	v_mov_b32_e32 v164, s64
	s_nop 0
	v_cndmask_b32_e64 v230, v162, v163, s[86:87]
	v_mov_b32_e32 v162, s63
	v_mov_b32_e32 v163, s65
	v_cndmask_b32_e64 v163, v162, v163, s[86:87]
	v_mov_b32_e32 v162, s62
	v_ashrrev_i32_e32 v231, 31, v230
	v_cndmask_b32_e64 v162, v162, v164, s[86:87]
	v_lshlrev_b64 v[164:165], 14, v[230:231]
	v_lshl_add_u64 v[162:163], v[162:163], 0, v[164:165]
	v_lshl_add_u64 v[162:163], v[162:163], 0, v[226:227]
	v_add_co_u32_e32 v194, vcc, s74, v162
	global_load_dwordx4 v[206:209], v[162:163], off
	global_load_dwordx4 v[190:193], v[162:163], off offset:1024
	global_load_dwordx4 v[186:189], v[162:163], off offset:2048
	global_load_dwordx4 v[178:181], v[162:163], off offset:3072
	v_addc_co_u32_e32 v195, vcc, 0, v163, vcc
	global_load_dwordx4 v[182:185], v[194:195], off offset:-4096
	v_add_co_u32_e32 v164, vcc, s72, v162
	s_nop 0
	s_nop 0
	v_addc_co_u32_e32 v165, vcc, 0, v163, vcc
	global_load_dwordx4 v[170:173], v[164:165], off offset:1024
	v_add_co_u32_e32 v196, vcc, s75, v162
	s_nop 0
	s_nop 0
	v_addc_co_u32_e32 v197, vcc, 0, v163, vcc
	global_load_dwordx4 v[222:225], v[164:165], off offset:2048
	global_load_dwordx4 v[210:213], v[164:165], off offset:3072
	global_load_dwordx4 v[198:201], v[194:195], off
	global_load_dwordx4 v[174:177], v[194:195], off offset:1024
	global_load_dwordx4 v[166:169], v[194:195], off offset:2048
	s_nop 0
	global_load_dwordx4 v[162:165], v[196:197], off offset:3072
	global_load_dwordx4 v[86:89], v[194:195], off offset:3072
	global_load_dwordx4 v[90:93], v[196:197], off
	global_load_dwordx4 v[94:97], v[196:197], off offset:1024
	global_load_dwordx4 v[98:101], v[196:197], off offset:2048
	s_waitcnt lgkmcnt(0)
	s_barrier
	ds_read_b128 v[2:5], v78
	ds_read_b128 v[6:9], v78 offset:64
	ds_read_b128 v[10:13], v77
	ds_read_b128 v[14:17], v77 offset:64
	s_waitcnt lgkmcnt(1)
	v_mfma_f32_16x16x32_bf16 v[2:5], v[2:5], v[10:13], 0
	ds_read_b128 v[18:21], v78 offset:128
	ds_read_b128 v[22:25], v78 offset:192
	s_waitcnt lgkmcnt(2)
	v_mfma_f32_16x16x32_bf16 v[2:5], v[6:9], v[14:17], v[2:5]
	ds_read_b128 v[6:9], v77 offset:128
	ds_read_b128 v[26:29], v77 offset:192
	s_waitcnt lgkmcnt(1)
	v_mfma_f32_16x16x32_bf16 v[2:5], v[18:21], v[6:9], v[2:5]
	s_waitcnt lgkmcnt(0)
	v_mfma_f32_16x16x32_bf16 v[2:5], v[22:25], v[26:29], v[2:5]
	s_nop 7
	ds_write_b32 v79, v2
	ds_write_b32 v79, v3 offset:1056
	ds_write_b32 v79, v4 offset:2112
	ds_write_b32 v79, v5 offset:3168
	ds_read_b128 v[2:5], v78 offset:8448
	ds_read_b128 v[18:21], v78 offset:8512
	s_waitcnt lgkmcnt(1)
	v_mfma_f32_16x16x32_bf16 v[2:5], v[2:5], v[10:13], 0
	ds_read_b128 v[10:13], v78 offset:8576
	s_waitcnt lgkmcnt(1)
	v_mfma_f32_16x16x32_bf16 v[2:5], v[18:21], v[14:17], v[2:5]
	ds_read_b128 v[14:17], v78 offset:8640
	s_waitcnt lgkmcnt(1)
	v_mfma_f32_16x16x32_bf16 v[2:5], v[10:13], v[6:9], v[2:5]
	s_waitcnt lgkmcnt(0)
	v_mfma_f32_16x16x32_bf16 v[2:5], v[14:17], v[26:29], v[2:5]
	s_nop 7
	ds_write_b32 v79, v2 offset:16896
	ds_write_b32 v79, v3 offset:17952
	ds_write_b32 v79, v4 offset:19008
	ds_write_b32 v79, v5 offset:20064
	ds_read_b128 v[2:5], v78 offset:256
	ds_read_b128 v[6:9], v78 offset:320
	ds_read_b128 v[10:13], v77 offset:34816
	ds_read_b128 v[14:17], v77 offset:34880
	s_waitcnt lgkmcnt(1)
	v_mfma_f32_16x16x32_bf16 v[2:5], v[2:5], v[10:13], 0
	ds_read_b128 v[18:21], v78 offset:384
	ds_read_b128 v[22:25], v78 offset:448
	s_waitcnt lgkmcnt(2)
	v_mfma_f32_16x16x32_bf16 v[2:5], v[6:9], v[14:17], v[2:5]
	ds_read_b128 v[6:9], v77 offset:34944
	ds_read_b128 v[26:29], v77 offset:35008
	s_waitcnt lgkmcnt(1)
	v_mfma_f32_16x16x32_bf16 v[2:5], v[18:21], v[6:9], v[2:5]
	s_waitcnt lgkmcnt(0)
	v_mfma_f32_16x16x32_bf16 v[2:5], v[22:25], v[26:29], v[2:5]
	s_nop 7
	ds_write_b32 v79, v2 offset:528
	ds_write_b32 v79, v3 offset:1584
	ds_write_b32 v79, v4 offset:2640
	ds_write_b32 v79, v5 offset:3696
	ds_read_b128 v[2:5], v78 offset:8704
	ds_read_b128 v[18:21], v78 offset:8768
	s_waitcnt lgkmcnt(1)
	v_mfma_f32_16x16x32_bf16 v[2:5], v[2:5], v[10:13], 0
	ds_read_b128 v[10:13], v78 offset:8832
	s_waitcnt lgkmcnt(1)
	v_mfma_f32_16x16x32_bf16 v[2:5], v[18:21], v[14:17], v[2:5]
	ds_read_b128 v[14:17], v78 offset:8896
	s_waitcnt lgkmcnt(1)
	v_mfma_f32_16x16x32_bf16 v[2:5], v[10:13], v[6:9], v[2:5]
	s_waitcnt lgkmcnt(0)
	v_mfma_f32_16x16x32_bf16 v[2:5], v[14:17], v[26:29], v[2:5]
	s_nop 7
	ds_write_b32 v79, v2 offset:17424
	ds_write_b32 v79, v3 offset:18480
	ds_write_b32 v79, v4 offset:19536
	ds_write_b32 v79, v5 offset:20592
	s_waitcnt lgkmcnt(0)
	s_barrier
	ds_read2_b32 v[8:9], v75 offset1:16
	ds_read2_b32 v[6:7], v75 offset0:32 offset1:48
	ds_read2_b32 v[4:5], v75 offset0:64 offset1:80
	ds_read2_b32 v[2:3], v75 offset0:96 offset1:112
	s_waitcnt lgkmcnt(3)
	v_not_b32_e32 v11, v8
	s_waitcnt lgkmcnt(2)
	v_not_b32_e32 v13, v6
	s_waitcnt lgkmcnt(1)
	v_not_b32_e32 v15, v4
	s_waitcnt lgkmcnt(0)
	v_not_b32_e32 v17, v2
	v_or_b32_e32 v25, 0x80000000, v2
	v_cmp_gt_i32_e32 vcc, 0, v2
	v_not_b32_e32 v16, v3
	v_or_b32_e32 v24, 0x80000000, v3
	v_cndmask_b32_e32 v17, v25, v17, vcc
	v_cmp_gt_i32_e32 vcc, 0, v3
	v_or_b32_e32 v23, 0x80000000, v4
	v_not_b32_e32 v14, v5
	v_cndmask_b32_e32 v16, v24, v16, vcc
	v_cmp_gt_i32_e32 vcc, 0, v4
	v_or_b32_e32 v22, 0x80000000, v5
	v_or_b32_e32 v21, 0x80000000, v6
	v_cndmask_b32_e32 v15, v23, v15, vcc
	v_cmp_gt_i32_e32 vcc, 0, v5
	v_not_b32_e32 v12, v7
	v_or_b32_e32 v20, 0x80000000, v7
	v_cndmask_b32_e32 v14, v22, v14, vcc
	v_cmp_gt_i32_e32 vcc, 0, v6
	v_or_b32_e32 v19, 0x80000000, v8
	v_not_b32_e32 v10, v9
	v_cndmask_b32_e32 v21, v21, v13, vcc
	v_cmp_gt_i32_e32 vcc, 0, v7
	v_or_b32_e32 v18, 0x80000000, v9
	s_nop 0
	v_cndmask_b32_e32 v12, v20, v12, vcc
	v_cmp_gt_i32_e32 vcc, 0, v8
	s_nop 1
	v_cndmask_b32_e32 v19, v19, v11, vcc
	v_cmp_gt_i32_e32 vcc, 0, v9
	s_nop 1
	v_cndmask_b32_e32 v18, v18, v10, vcc
	v_max_u32_e32 v10, v18, v19
	v_max3_u32 v10, v12, v21, v10
	v_max3_u32 v10, v14, v15, v10
	v_max3_u32 v10, v16, v17, v10
	s_nop 1
	v_max_u32_dpp v11, v10, v10 row_ror:8 row_mask:0xf bank_mask:0xf bound_ctrl:1
	v_min_u32_dpp v10, v10, v10 row_ror:8 row_mask:0xf bank_mask:0xf bound_ctrl:1
	s_nop 0
	v_max_u32_dpp v11, v11, v11 row_ror:4 row_mask:0xf bank_mask:0xf bound_ctrl:1
	v_min_u32_dpp v10, v10, v10 row_ror:4 row_mask:0xf bank_mask:0xf bound_ctrl:1
	s_nop 0
	v_max_u32_dpp v11, v11, v11 row_ror:2 row_mask:0xf bank_mask:0xf bound_ctrl:1
	v_min_u32_dpp v10, v10, v10 row_ror:2 row_mask:0xf bank_mask:0xf bound_ctrl:1
	s_nop 0
	v_max_u32_dpp v20, v11, v11 row_ror:1 row_mask:0xf bank_mask:0xf bound_ctrl:1
	v_min_u32_dpp v10, v10, v10 row_ror:1 row_mask:0xf bank_mask:0xf bound_ctrl:1
	v_sub_u32_e64 v22, v10, 1 clamp
	v_sub_u32_e64 v13, v14, v22 clamp
	v_sub_u32_e64 v14, v15, v22 clamp
	v_sub_u32_e64 v15, v12, v22 clamp
	v_sub_u32_e32 v12, v20, v22
	v_ffbh_u32_e32 v12, v12
	v_xor_b32_e32 v12, 31, v12
	v_sub_u32_e64 v11, v17, v22 clamp
	v_readlane_b32 s6, v12, 0
	v_readlane_b32 s7, v12, 16
	v_readlane_b32 s8, v12, 32
	s_max_i32 s6, s7, s6
	v_sub_u32_e64 v17, v18, v22 clamp
	v_readlane_b32 s9, v12, 48
	v_mov_b32_e32 v12, s8
	v_mov_b32_e32 v18, s6
	v_max3_i32 v12, s9, v12, v18
	v_cmp_lt_i32_e32 vcc, -1, v12
	v_sub_u32_e64 v10, v16, v22 clamp
	v_sub_u32_e64 v16, v21, v22 clamp
	v_sub_u32_e64 v19, v19, v22 clamp
	v_readfirstlane_b32 s16, v12
	s_mov_b64 s[6:7], -1
	s_cbranch_vccnz .LBB0_1811
	s_mov_b64 s[6:7], 0
